# baseline (speedup 1.0000x reference)
.LBB3_1:
	s_movk_i32 s6, 0x200
	s_add_i32 s2, s6, s2
	s_ashr_i32 s30, s2, 3
	s_ashr_i32 s31, s30, 31
	s_lshr_b32 s31, s31, 29
	s_lshl_b32 s6, s2, 4
	s_add_i32 s31, s30, s31
	s_and_b32 s6, s6, 0x70
	s_ashr_i32 s34, s31, 3
	s_and_b32 s31, s31, 0x1fffff8
	s_add_i32 s34, s6, s34
	s_mul_i32 s54, s34, 0x12000
	s_mul_hi_i32 s55, s34, 0x12000
	s_add_u32 s46, s50, s54
	s_addc_u32 s47, s51, s55
	s_add_u32 s48, s52, s54
	s_addc_u32 s49, s53, s55
	s_sub_i32 s6, s30, s31
	v_lshl_or_b32 v80, s6, 7, v192
	s_add_u32 s6, s40, 0x0
	v_mad_i64_i32 v[174:175], s[30:31], s34, v202, v[178:179]
	s_mov_b32 m0, s6
	s_add_u32 s6, s40, 0x8000
	v_mad_i64_i32 v[176:177], s[30:31], s34, v202, v[180:181]
	global_load_lds_dwordx4 v[174:175], off
	s_mov_b32 m0, s6
	s_add_u32 s6, s40, 0x2000
	global_load_lds_dwordx4 v[176:177], off
	v_lshl_add_u64 v[82:83], v[174:175], 0, s[8:9]
	s_mov_b32 m0, s6
	s_add_u32 s6, s40, 0x4000
	s_ashr_i32 s35, s34, 31
	global_load_lds_dwordx4 v[82:83], off
	v_lshl_add_u64 v[82:83], v[174:175], 0, s[10:11]
	s_mov_b32 m0, s6
	s_add_u32 s6, s40, 0xa000
	global_load_lds_dwordx4 v[82:83], off
	v_lshl_add_u64 v[82:83], v[176:177], 0, 64
	s_mov_b32 m0, s6
	s_lshl_b64 s[30:31], s[34:35], 10
	v_ashrrev_i32_e32 v81, 31, v80
	global_load_lds_dwordx4 v[82:83], off
	v_lshl_add_u64 v[82:83], s[30:31], 0, v[80:81]
	v_or_b32_e32 v82, v82, v168
	v_lshlrev_b64 v[82:83], 6, v[82:83]
	v_lshl_add_u64 v[82:83], v[182:183], 0, v[82:83]
	global_load_dwordx4 v[152:155], v[82:83], off
	global_load_dwordx4 v[156:159], v[82:83], off offset:16

	.amdhsa_kernel _Z13attn11_kernelILi4EEvPc
		.amdhsa_group_segment_fixed_size 16384
		.amdhsa_private_segment_fixed_size 0
		.amdhsa_kernarg_size 264
		.amdhsa_user_sgpr_count 2
		.amdhsa_user_sgpr_dispatch_ptr 0
		.amdhsa_user_sgpr_queue_ptr 0
		.amdhsa_user_sgpr_kernarg_segment_ptr 1
		.amdhsa_user_sgpr_dispatch_id 0
		.amdhsa_user_sgpr_kernarg_preload_length 0
		.amdhsa_user_sgpr_kernarg_preload_offset 0
		.amdhsa_user_sgpr_private_segment_size 0
		.amdhsa_uses_dynamic_stack 0
		.amdhsa_enable_private_segment 0
		.amdhsa_system_sgpr_workgroup_id_x 1
		.amdhsa_system_sgpr_workgroup_id_y 0
		.amdhsa_system_sgpr_workgroup_id_z 0
		.amdhsa_system_sgpr_workgroup_info 0
		.amdhsa_system_vgpr_workitem_id 0
		.amdhsa_next_free_vgpr 228
		.amdhsa_next_free_sgpr 58
		.amdhsa_accum_offset 228
		.amdhsa_reserve_vcc 1
		.amdhsa_float_round_mode_32 0
		.amdhsa_float_round_mode_16_64 0
		.amdhsa_float_denorm_mode_32 3
		.amdhsa_float_denorm_mode_16_64 3
		.amdhsa_dx10_clamp 1
		.amdhsa_ieee_mode 1
		.amdhsa_fp16_overflow 0
		.amdhsa_tg_split 0
		.amdhsa_exception_fp_ieee_invalid_op 0
		.amdhsa_exception_fp_denorm_src 0
		.amdhsa_exception_fp_ieee_div_zero 0
		.amdhsa_exception_fp_ieee_overflow 0
		.amdhsa_exception_fp_ieee_underflow 0
		.amdhsa_exception_fp_ieee_inexact 0
		.amdhsa_exception_int_div_zero 0
	.end_amdhsa_kernel

amdhsa.kernels:
  - .agpr_count:     0
    .args:
      - .actual_access:  read_only
        .address_space:  global
        .offset:         0
        .size:           8
        .value_kind:     global_buffer
      - .actual_access:  read_only
        .address_space:  global
        .offset:         8
        .size:           8
        .value_kind:     global_buffer
      - .actual_access:  read_only
        .address_space:  global
        .offset:         16
        .size:           8
        .value_kind:     global_buffer
      - .actual_access:  read_only
        .address_space:  global
        .offset:         24
        .size:           8
        .value_kind:     global_buffer
      - .actual_access:  read_only
        .address_space:  global
        .offset:         32
        .size:           8
        .value_kind:     global_buffer
      - .actual_access:  read_only
        .address_space:  global
        .offset:         40
        .size:           8
        .value_kind:     global_buffer
      - .actual_access:  read_only
        .address_space:  global
        .offset:         48
        .size:           8
        .value_kind:     global_buffer
      - .actual_access:  write_only
        .address_space:  global
        .offset:         56
        .size:           8
        .value_kind:     global_buffer
    .group_segment_fixed_size: 32
    .kernarg_segment_align: 8
    .kernarg_segment_size: 64
    .language:       OpenCL C
    .language_version:
      - 2
      - 0
    .max_flat_workgroup_size: 256
    .name:           _Z11prep_kernelPKfS0_S0_S0_S0_S0_S0_Pc
    .private_segment_fixed_size: 0
    .sgpr_count:     48
    .sgpr_spill_count: 0
    .symbol:         _Z11prep_kernelPKfS0_S0_S0_S0_S0_S0_Pc.kd
    .uniform_work_group_size: 1
    .uses_dynamic_stack: false
    .vgpr_count:     78
    .vgpr_spill_count: 0
    .wavefront_size: 64
  - .agpr_count:     0
    .args:
      - .address_space:  global
        .offset:         0
        .size:           8
        .value_kind:     global_buffer
      - .actual_access:  read_only
        .address_space:  global
        .offset:         8
        .size:           8
        .value_kind:     global_buffer
      - .actual_access:  read_only
        .address_space:  global
        .offset:         16
        .size:           8
        .value_kind:     global_buffer
    .group_segment_fixed_size: 0
    .kernarg_segment_align: 8
    .kernarg_segment_size: 24
    .language:       OpenCL C
    .language_version:
      - 2
      - 0
    .max_flat_workgroup_size: 512
    .name:           _Z13qkv256_kernelPcPKfS1_
    .private_segment_fixed_size: 0
    .sgpr_count:     35
    .sgpr_spill_count: 0
    .symbol:         _Z13qkv256_kernelPcPKfS1_.kd
    .uniform_work_group_size: 1
    .uses_dynamic_stack: false
    .vgpr_count:     214
    .vgpr_spill_count: 0
    .wavefront_size: 64
  - .agpr_count:     0
    .args:
      - .address_space:  global
        .offset:         0
        .size:           8
        .value_kind:     global_buffer
      - .actual_access:  read_only
        .address_space:  global
        .offset:         8
        .size:           8
        .value_kind:     global_buffer
      - .actual_access:  read_only
        .address_space:  global
        .offset:         16
        .size:           8
        .value_kind:     global_buffer
      - .actual_access:  write_only
        .address_space:  global
        .offset:         24
        .size:           8
        .value_kind:     global_buffer
    .group_segment_fixed_size: 0
    .kernarg_segment_align: 8
    .kernarg_segment_size: 32
    .language:       OpenCL C
    .language_version:
      - 2
      - 0
    .max_flat_workgroup_size: 256
    .name:           _Z11proj_kernelPKcPKfS2_Pf
    .private_segment_fixed_size: 0
    .sgpr_count:     34
    .sgpr_spill_count: 0
    .symbol:         _Z11proj_kernelPKcPKfS2_Pf.kd
    .uniform_work_group_size: 1
    .uses_dynamic_stack: false
    .vgpr_count:     185
    .vgpr_spill_count: 0
    .wavefront_size: 64
  - .agpr_count:     0
    .args:
      - .address_space:  global
        .offset:         0
        .size:           8
        .value_kind:     global_buffer
      - .offset:         8
        .size:           4
        .value_kind:     hidden_block_count_x
      - .offset:         12
        .size:           4
        .value_kind:     hidden_block_count_y
      - .offset:         16
        .size:           4
        .value_kind:     hidden_block_count_z
      - .offset:         20
        .size:           2
        .value_kind:     hidden_group_size_x
      - .offset:         22
        .size:           2
        .value_kind:     hidden_group_size_y
      - .offset:         24
        .size:           2
        .value_kind:     hidden_group_size_z
      - .offset:         26
        .size:           2
        .value_kind:     hidden_remainder_x
      - .offset:         28
        .size:           2
        .value_kind:     hidden_remainder_y
      - .offset:         30
        .size:           2
        .value_kind:     hidden_remainder_z
      - .offset:         48
        .size:           8
        .value_kind:     hidden_global_offset_x
      - .offset:         56
        .size:           8
        .value_kind:     hidden_global_offset_y
      - .offset:         64
        .size:           8
        .value_kind:     hidden_global_offset_z
      - .offset:         72
        .size:           2
        .value_kind:     hidden_grid_dims
      - .offset:         128
        .size:           4
        .value_kind:     hidden_dynamic_lds_size
    .group_segment_fixed_size: 16384
    .kernarg_segment_align: 8
    .kernarg_segment_size: 264
    .language:       OpenCL C
    .language_version:
      - 2
      - 0
    .max_flat_workgroup_size: 256
    .name:           _Z13attn11_kernelILi4EEvPc
    .private_segment_fixed_size: 0
    .sgpr_count:     64
    .sgpr_spill_count: 0
    .symbol:         _Z13attn11_kernelILi4EEvPc.kd
    .uniform_work_group_size: 1
    .uses_dynamic_stack: false
    .vgpr_count:     228
    .vgpr_spill_count: 0
    .wavefront_size: 64
